# v79 + final f32 output stores of the last combine phase marked non-temporal (never re-read by the kernel)
# speedup vs baseline: 1.0033x; 1.0033x over previous
; __device__ __forceinline__ float bf2f(bf16_t h) { return __uint_as_float(((unsigned)h) << 16); }
; __device__ __forceinline__ void ph_combine(const Args& a, const bf16_t* X, const float* g, const float* b, bf16_t* Xo, float* outf) {
;     ...
;     for (int row = gw; row < M; row += ngw) {
;         float v[16];
; #pragma unroll
;         for (int j = 0; j < 16; ++j) v[j] = 0.f;
;         u32x2 q0[YB_NSLOT], q1[YB_NSLOT];
; #pragma unroll
;         for (int k = 0; k < YB_NSLOT; ++k) { const unsigned char* yr = YB + ((size_t)row * 10 + k) * 1024; q0[k] = __builtin_nontemporal_load((const u32x2*)(yr + lane * 8)); q1[k] = __builtin_nontemporal_load((const u32x2*)(yr + 512 + lane * 8)); }
; #pragma unroll
;         for (int k = 0; k < YB_NSLOT; ++k) {
;             const auto a0 = __builtin_amdgcn_cvt_pk_f32_fp8((int)q0[k].x, false), a1 = __builtin_amdgcn_cvt_pk_f32_fp8((int)q0[k].x, true), a2 = __builtin_amdgcn_cvt_pk_f32_fp8((int)q0[k].y, false), a3 = __builtin_amdgcn_cvt_pk_f32_fp8((int)q0[k].y, true);
;             const auto b0 = __builtin_amdgcn_cvt_pk_f32_fp8((int)q1[k].x, false), b1 = __builtin_amdgcn_cvt_pk_f32_fp8((int)q1[k].x, true), b2 = __builtin_amdgcn_cvt_pk_f32_fp8((int)q1[k].y, false), b3 = __builtin_amdgcn_cvt_pk_f32_fp8((int)q1[k].y, true);
;             v[0] += a0[0]; v[1] += a0[1]; v[2] += a1[0]; v[3] += a1[1]; v[4] += a2[0]; v[5] += a2[1]; v[6] += a3[0]; v[7] += a3[1];
;             v[8] += b0[0]; v[9] += b0[1]; v[10] += b1[0]; v[11] += b1[1]; v[12] += b2[0]; v[13] += b2[1]; v[14] += b3[0]; v[15] += b3[1];
;         }
;         {
;             const bf16x8 p0 = *(const bf16x8*)(X + (size_t)row * 1024 + lane * 8), p1 = *(const bf16x8*)(X + (size_t)row * 1024 + 512 + lane * 8);
; #pragma unroll
;             for (int j = 0; j < 8; ++j) { v[j] = v[j] * (1.0f / YB_SCALE) + ALPHA * bf2f((bf16_t)p0[j]); v[8 + j] = v[8 + j] * (1.0f / YB_SCALE) + ALPHA * bf2f((bf16_t)p1[j]); }
.LBB0_2918:
	v_lshl_add_u64 v[0:1], s[2:3], 0, v[26:27]
	v_add_co_u32_e32 v2, vcc, 0x19b00000, v0
	s_nop 1
	v_addc_co_u32_e32 v3, vcc, 0, v1, vcc
	global_load_dwordx2 v[4:5], v[2:3], off nt
	global_load_dwordx2 v[6:7], v[2:3], off offset:512 nt
	global_load_dwordx2 v[8:9], v[2:3], off offset:1024 nt
	global_load_dwordx2 v[10:11], v[2:3], off offset:1536 nt
	global_load_dwordx2 v[38:39], v[2:3], off offset:2048 nt
	global_load_dwordx2 v[40:41], v[2:3], off offset:2560 nt
	global_load_dwordx2 v[42:43], v[2:3], off offset:3072 nt
	v_add_co_u32_e32 v30, vcc, 0x19b01000, v0
	global_load_dwordx2 v[44:45], v[2:3], off offset:3584 nt
	s_nop 0
	v_addc_co_u32_e32 v31, vcc, 0, v1, vcc
	global_load_dwordx2 v[46:47], v[30:31], off nt
	global_load_dwordx2 v[48:49], v[30:31], off offset:512 nt
	global_load_dwordx2 v[50:51], v[30:31], off offset:1024 nt
	global_load_dwordx2 v[52:53], v[30:31], off offset:1536 nt
	global_load_dwordx2 v[54:55], v[30:31], off offset:2048 nt
	global_load_dwordx2 v[56:57], v[30:31], off offset:2560 nt
	global_load_dwordx2 v[58:59], v[30:31], off offset:3072 nt
	v_add_co_u32_e32 v0, vcc, 0x19b02000, v0
	global_load_dwordx2 v[60:61], v[30:31], off offset:3584 nt
	s_nop 0
	v_addc_co_u32_e32 v1, vcc, 0, v1, vcc
	global_load_dwordx2 v[62:63], v[0:1], off nt
	global_load_dwordx2 v[64:65], v[0:1], off offset:512 nt
	s_waitcnt vmcnt(0)
	v_cvt_pk_f32_fp8_e32 v[68:69], v4
	v_cvt_pk_f32_fp8_sdwa v[76:77], v4 src0_sel:WORD_1
	v_cvt_pk_f32_fp8_e32 v[96:97], v5
	v_cvt_pk_f32_fp8_sdwa v[100:101], v5 src0_sel:WORD_1
	s_waitcnt vmcnt(15)
	v_cvt_pk_f32_fp8_e32 v[102:103], v8
	v_cvt_pk_f32_fp8_sdwa v[104:105], v8 src0_sel:WORD_1
	v_cvt_pk_f32_fp8_e32 v[106:107], v9
	v_cvt_pk_f32_fp8_sdwa v[108:109], v9 src0_sel:WORD_1
	s_waitcnt vmcnt(13)
	v_cvt_pk_f32_fp8_e32 v[114:115], v39
	v_cvt_pk_f32_fp8_sdwa v[116:117], v39 src0_sel:WORD_1
	s_waitcnt vmcnt(11)
	v_cvt_pk_f32_fp8_e32 v[122:123], v43
	v_cvt_pk_f32_fp8_sdwa v[124:125], v43 src0_sel:WORD_1
	v_mov_b32_e32 v67, v76
	v_mov_b32_e32 v76, v69
	s_waitcnt vmcnt(9)
	v_cvt_pk_f32_fp8_e32 v[130:131], v47
	v_cvt_pk_f32_fp8_sdwa v[132:133], v47 src0_sel:WORD_1
	v_mov_b32_e32 v66, v68
	v_pk_add_f32 v[68:69], v[76:77], 0 op_sel_hi:[1,0]
	v_mov_b32_e32 v76, v96
	v_mov_b32_e32 v77, v100
	s_waitcnt vmcnt(7)
	v_cvt_pk_f32_fp8_e32 v[138:139], v51
	v_cvt_pk_f32_fp8_sdwa v[140:141], v51 src0_sel:WORD_1
	v_mov_b32_e32 v166, v102
	v_mov_b32_e32 v167, v104
	v_mov_b32_e32 v104, v103
	v_pk_add_f32 v[76:77], v[76:77], 0 op_sel_hi:[1,0]
	v_mov_b32_e32 v102, v106
	v_mov_b32_e32 v103, v108
	s_waitcnt vmcnt(5)
	v_cvt_pk_f32_fp8_e32 v[146:147], v55
	v_cvt_pk_f32_fp8_sdwa v[148:149], v55 src0_sel:WORD_1
	v_pk_add_f32 v[76:77], v[76:77], v[102:103]
	v_mov_b32_e32 v102, v114
	v_mov_b32_e32 v103, v116
	s_waitcnt vmcnt(3)
	v_cvt_pk_f32_fp8_e32 v[154:155], v59
	v_cvt_pk_f32_fp8_sdwa v[156:157], v59 src0_sel:WORD_1
	v_pk_add_f32 v[76:77], v[76:77], v[102:103]
	v_mov_b32_e32 v102, v122
	v_mov_b32_e32 v103, v124
	v_cvt_pk_f32_fp8_e32 v[0:1], v6
	v_cvt_pk_f32_fp8_sdwa v[2:3], v6 src0_sel:WORD_1
	s_waitcnt vmcnt(1)
	v_cvt_pk_f32_fp8_e32 v[162:163], v63
	v_cvt_pk_f32_fp8_sdwa v[164:165], v63 src0_sel:WORD_1
	v_pk_add_f32 v[76:77], v[76:77], v[102:103]
	v_mov_b32_e32 v102, v130
	v_mov_b32_e32 v103, v132
	v_cvt_pk_f32_fp8_e32 v[30:31], v7
	v_cvt_pk_f32_fp8_sdwa v[32:33], v7 src0_sel:WORD_1
	v_cvt_pk_f32_fp8_e32 v[4:5], v10
	v_cvt_pk_f32_fp8_sdwa v[6:7], v10 src0_sel:WORD_1
	v_pk_add_f32 v[76:77], v[76:77], v[102:103]
	v_mov_b32_e32 v102, v138
	v_mov_b32_e32 v103, v140
	v_cvt_pk_f32_fp8_e32 v[34:35], v11
	v_cvt_pk_f32_fp8_sdwa v[36:37], v11 src0_sel:WORD_1
	v_cvt_pk_f32_fp8_e32 v[8:9], v40
	v_cvt_pk_f32_fp8_sdwa v[10:11], v40 src0_sel:WORD_1
	v_pk_add_f32 v[76:77], v[76:77], v[102:103]
	v_mov_b32_e32 v102, v146
	v_mov_b32_e32 v103, v148
	v_cvt_pk_f32_fp8_e32 v[84:85], v44
	v_cvt_pk_f32_fp8_sdwa v[86:87], v44 src0_sel:WORD_1
	v_pk_add_f32 v[76:77], v[76:77], v[102:103]
	v_mov_b32_e32 v102, v154
	v_mov_b32_e32 v103, v156
	v_mov_b32_e32 v100, v97
	v_cvt_pk_f32_fp8_e32 v[92:93], v48
	v_cvt_pk_f32_fp8_sdwa v[94:95], v48 src0_sel:WORD_1
	v_pk_add_f32 v[76:77], v[76:77], v[102:103]
	v_mov_b32_e32 v102, v162
	v_mov_b32_e32 v103, v164
	v_pk_add_f32 v[96:97], v[100:101], 0 op_sel_hi:[1,0]
	v_mov_b32_e32 v100, v0
	v_mov_b32_e32 v101, v2
	v_cvt_pk_f32_fp8_e32 v[72:73], v52
	v_cvt_pk_f32_fp8_sdwa v[70:71], v52 src0_sel:WORD_1
	v_pk_add_f32 v[76:77], v[76:77], v[102:103]
	v_pk_add_f32 v[100:101], v[100:101], 0 op_sel_hi:[1,0]
	v_mov_b32_e32 v102, v4
	v_mov_b32_e32 v103, v6
	v_pk_add_f32 v[100:101], v[100:101], v[102:103]
	v_mov_b32_e32 v102, v8
	v_mov_b32_e32 v103, v10
	v_pk_add_f32 v[100:101], v[100:101], v[102:103]
	v_mov_b32_e32 v102, v84
	v_mov_b32_e32 v103, v86
	v_pk_add_f32 v[100:101], v[100:101], v[102:103]
	v_mov_b32_e32 v102, v92
	v_mov_b32_e32 v103, v94
	v_cvt_pk_f32_fp8_e32 v[74:75], v56
	v_cvt_pk_f32_fp8_sdwa v[78:79], v56 src0_sel:WORD_1
	v_pk_add_f32 v[100:101], v[100:101], v[102:103]
	v_mov_b32_e32 v102, v72
	v_mov_b32_e32 v103, v70
	v_cvt_pk_f32_fp8_e32 v[110:111], v38
	v_cvt_pk_f32_fp8_sdwa v[112:113], v38 src0_sel:WORD_1
	v_pk_add_f32 v[68:69], v[68:69], v[104:105]
	v_mov_b32_e32 v108, v107
	v_pk_add_f32 v[104:105], v[100:101], v[102:103]
	v_lshl_add_u64 v[100:101], s[2:3], 0, v[24:25]
	v_pk_add_f32 v[96:97], v[96:97], v[108:109]
	v_add_co_u32_e32 v108, vcc, s11, v100
	v_pk_add_f32 v[66:67], v[66:67], 0 op_sel_hi:[1,0]
	s_nop 0
	v_addc_co_u32_e32 v109, vcc, 0, v101, vcc
	v_mov_b32_e32 v106, v74
	v_mov_b32_e32 v107, v78
	global_load_dwordx4 v[100:103], v[108:109], off
	v_pk_add_f32 v[66:67], v[66:67], v[166:167]
	v_mov_b32_e32 v166, v110
	v_mov_b32_e32 v167, v112
	v_mov_b32_e32 v112, v111
	v_pk_add_f32 v[110:111], v[104:105], v[106:107]
	global_load_dwordx4 v[104:107], v[108:109], off offset:1024
	v_mov_b32_e32 v2, v1
	v_pk_add_f32 v[0:1], v[2:3], 0 op_sel_hi:[1,0]
	v_mov_b32_e32 v6, v5
	v_pk_add_f32 v[0:1], v[0:1], v[6:7]
	v_mov_b32_e32 v10, v9
	v_pk_add_f32 v[0:1], v[0:1], v[10:11]
	v_mov_b32_e32 v86, v85
	v_pk_add_f32 v[0:1], v[0:1], v[86:87]
	v_mov_b32_e32 v94, v93
	v_pk_add_f32 v[92:93], v[0:1], v[94:95]
	global_load_dwordx4 v[0:3], v[18:19], off offset:16
	global_load_dwordx4 v[8:11], v[18:19], off
	v_cvt_pk_f32_fp8_e32 v[80:81], v60
	v_cvt_pk_f32_fp8_sdwa v[82:83], v60 src0_sel:WORD_1
	s_waitcnt vmcnt(4)
; __device__ __forceinline__ float bf2f(bf16_t h) { return __uint_as_float(((unsigned)h) << 16); }
; __device__ __forceinline__ void ph_combine(const Args& a, const bf16_t* X, const float* g, const float* b, bf16_t* Xo, float* outf) {
;     ...
;         for (int k = 0; k < YB_NSLOT; ++k) { const unsigned char* yr = YB + ((size_t)row * 10 + k) * 1024; q0[k] = __builtin_nontemporal_load((const u32x2*)(yr + lane * 8)); q1[k] = __builtin_nontemporal_load((const u32x2*)(yr + 512 + lane * 8)); }
; #pragma unroll
;         for (int k = 0; k < YB_NSLOT; ++k) {
;             const auto a0 = __builtin_amdgcn_cvt_pk_f32_fp8((int)q0[k].x, false), a1 = __builtin_amdgcn_cvt_pk_f32_fp8((int)q0[k].x, true), a2 = __builtin_amdgcn_cvt_pk_f32_fp8((int)q0[k].y, false), a3 = __builtin_amdgcn_cvt_pk_f32_fp8((int)q0[k].y, true);
;             const auto b0 = __builtin_amdgcn_cvt_pk_f32_fp8((int)q1[k].x, false), b1 = __builtin_amdgcn_cvt_pk_f32_fp8((int)q1[k].x, true), b2 = __builtin_amdgcn_cvt_pk_f32_fp8((int)q1[k].y, false), b3 = __builtin_amdgcn_cvt_pk_f32_fp8((int)q1[k].y, true);
;             v[0] += a0[0]; v[1] += a0[1]; v[2] += a1[0]; v[3] += a1[1]; v[4] += a2[0]; v[5] += a2[1]; v[6] += a3[0]; v[7] += a3[1];
;             v[8] += b0[0]; v[9] += b0[1]; v[10] += b1[0]; v[11] += b1[1]; v[12] += b2[0]; v[13] += b2[1]; v[14] += b3[0]; v[15] += b3[1];
;         }
;         {
;             const bf16x8 p0 = *(const bf16x8*)(X + (size_t)row * 1024 + lane * 8), p1 = *(const bf16x8*)(X + (size_t)row * 1024 + 512 + lane * 8);
; #pragma unroll
;             for (int j = 0; j < 8; ++j) { v[j] = v[j] * (1.0f / YB_SCALE) + ALPHA * bf2f((bf16_t)p0[j]); v[8 + j] = v[8 + j] * (1.0f / YB_SCALE) + ALPHA * bf2f((bf16_t)p1[j]); }
;         }
;         float s = 0.f;
; #pragma unroll
;         for (int j = 0; j < 16; ++j) s += v[j];
	v_cvt_pk_f32_fp8_e32 v[88:89], v64
	v_cvt_pk_f32_fp8_sdwa v[90:91], v64 src0_sel:WORD_1
	v_mov_b32_e32 v70, v73
	v_pk_add_f32 v[70:71], v[92:93], v[70:71]
	v_mov_b32_e32 v78, v75
	v_mov_b32_e32 v108, v80
	v_mov_b32_e32 v109, v82
	v_pk_add_f32 v[70:71], v[70:71], v[78:79]
	v_mov_b32_e32 v82, v81
	v_pk_add_f32 v[108:109], v[110:111], v[108:109]
	v_mov_b32_e32 v111, v90
	v_pk_add_f32 v[70:71], v[70:71], v[82:83]
	v_mov_b32_e32 v90, v89
	v_pk_add_f32 v[74:75], v[70:71], v[90:91]
	v_mov_b32_e32 v70, v30
	v_mov_b32_e32 v71, v32
	v_pk_add_f32 v[70:71], v[70:71], 0 op_sel_hi:[1,0]
	v_mov_b32_e32 v72, v34
	v_mov_b32_e32 v73, v36
	v_mov_b32_e32 v110, v88
	global_load_dwordx4 v[4:7], v[20:21], off offset:16
	global_load_dwordx4 v[84:87], v[20:21], off
	v_pk_add_f32 v[82:83], v[70:71], v[72:73]
	global_load_dwordx4 v[70:73], v[14:15], off offset:16
	global_load_dwordx4 v[78:81], v[14:15], off
	global_load_dwordx4 v[88:91], v[16:17], off offset:16
	global_load_dwordx4 v[92:95], v[16:17], off
	v_cvt_pk_f32_fp8_e32 v[38:39], v41
	v_cvt_pk_f32_fp8_sdwa v[40:41], v41 src0_sel:WORD_1
	v_cvt_pk_f32_fp8_e32 v[118:119], v42
	v_cvt_pk_f32_fp8_sdwa v[120:121], v42 src0_sel:WORD_1
	v_cvt_pk_f32_fp8_e32 v[42:43], v45
	v_cvt_pk_f32_fp8_sdwa v[44:45], v45 src0_sel:WORD_1
	v_cvt_pk_f32_fp8_e32 v[126:127], v46
	v_cvt_pk_f32_fp8_sdwa v[128:129], v46 src0_sel:WORD_1
	v_cvt_pk_f32_fp8_e32 v[46:47], v49
	v_cvt_pk_f32_fp8_sdwa v[48:49], v49 src0_sel:WORD_1
	v_cvt_pk_f32_fp8_e32 v[134:135], v50
	v_cvt_pk_f32_fp8_sdwa v[136:137], v50 src0_sel:WORD_1
	v_mov_b32_e32 v32, v31
	v_cvt_pk_f32_fp8_e32 v[50:51], v53
	v_cvt_pk_f32_fp8_sdwa v[52:53], v53 src0_sel:WORD_1
	v_cvt_pk_f32_fp8_e32 v[142:143], v54
	v_cvt_pk_f32_fp8_sdwa v[144:145], v54 src0_sel:WORD_1
	v_pk_add_f32 v[30:31], v[32:33], 0 op_sel_hi:[1,0]
	v_mov_b32_e32 v36, v35
	v_cvt_pk_f32_fp8_e32 v[54:55], v57
	v_cvt_pk_f32_fp8_sdwa v[56:57], v57 src0_sel:WORD_1
	v_cvt_pk_f32_fp8_e32 v[150:151], v58
	v_cvt_pk_f32_fp8_sdwa v[152:153], v58 src0_sel:WORD_1
	v_pk_add_f32 v[66:67], v[66:67], v[166:167]
	v_mov_b32_e32 v166, v118
	v_mov_b32_e32 v167, v120
	v_pk_add_f32 v[108:109], v[108:109], v[110:111]
	v_mov_b32_e32 v110, v38
	v_mov_b32_e32 v111, v40
	v_pk_add_f32 v[30:31], v[30:31], v[36:37]
	v_mov_b32_e32 v40, v39
	v_cvt_pk_f32_fp8_e32 v[58:59], v61
	v_cvt_pk_f32_fp8_sdwa v[60:61], v61 src0_sel:WORD_1
	v_cvt_pk_f32_fp8_e32 v[158:159], v62
	v_cvt_pk_f32_fp8_sdwa v[160:161], v62 src0_sel:WORD_1
	v_pk_add_f32 v[66:67], v[66:67], v[166:167]
	v_mov_b32_e32 v166, v126
	v_mov_b32_e32 v167, v128
	v_pk_add_f32 v[68:69], v[68:69], v[112:113]
	v_mov_b32_e32 v120, v119
	v_pk_add_f32 v[82:83], v[82:83], v[110:111]
	v_mov_b32_e32 v110, v42
	v_mov_b32_e32 v111, v44
	v_pk_add_f32 v[30:31], v[30:31], v[40:41]
	v_mov_b32_e32 v44, v43
	v_cvt_pk_f32_fp8_e32 v[62:63], v65
	v_cvt_pk_f32_fp8_sdwa v[64:65], v65 src0_sel:WORD_1
	v_pk_add_f32 v[66:67], v[66:67], v[166:167]
	v_mov_b32_e32 v166, v134
	v_mov_b32_e32 v167, v136
	v_pk_add_f32 v[68:69], v[68:69], v[120:121]
	v_mov_b32_e32 v128, v127
	v_pk_add_f32 v[82:83], v[82:83], v[110:111]
	v_mov_b32_e32 v110, v46
	v_mov_b32_e32 v111, v48
	v_pk_add_f32 v[30:31], v[30:31], v[44:45]
	v_mov_b32_e32 v48, v47
	v_pk_add_f32 v[66:67], v[66:67], v[166:167]
	v_mov_b32_e32 v166, v142
	v_mov_b32_e32 v167, v144
	v_pk_add_f32 v[68:69], v[68:69], v[128:129]
	v_mov_b32_e32 v136, v135
	v_pk_add_f32 v[82:83], v[82:83], v[110:111]
	v_mov_b32_e32 v110, v50
	v_mov_b32_e32 v111, v52
	v_pk_add_f32 v[30:31], v[30:31], v[48:49]
	v_mov_b32_e32 v52, v51
	v_pk_add_f32 v[66:67], v[66:67], v[166:167]
	v_mov_b32_e32 v166, v150
	v_mov_b32_e32 v167, v152
	v_pk_add_f32 v[68:69], v[68:69], v[136:137]
	v_mov_b32_e32 v144, v143
	v_mov_b32_e32 v116, v115
	v_pk_add_f32 v[82:83], v[82:83], v[110:111]
	v_mov_b32_e32 v110, v54
	v_mov_b32_e32 v111, v56
	v_pk_add_f32 v[30:31], v[30:31], v[52:53]
	v_mov_b32_e32 v56, v55
	v_pk_add_f32 v[66:67], v[66:67], v[166:167]
	v_mov_b32_e32 v166, v158
	v_mov_b32_e32 v167, v160
	v_pk_add_f32 v[68:69], v[68:69], v[144:145]
	v_mov_b32_e32 v152, v151
	v_pk_add_f32 v[96:97], v[96:97], v[116:117]
	v_mov_b32_e32 v124, v123
	v_pk_add_f32 v[82:83], v[82:83], v[110:111]
	v_mov_b32_e32 v110, v58
	v_mov_b32_e32 v111, v60
	v_pk_add_f32 v[30:31], v[30:31], v[56:57]
	v_mov_b32_e32 v60, v59
	s_waitcnt vmcnt(0)
	v_lshlrev_b32_e32 v33, 16, v101
	v_lshlrev_b32_e32 v32, 16, v100
	v_pk_add_f32 v[66:67], v[66:67], v[166:167]
	v_pk_add_f32 v[68:69], v[68:69], v[152:153]
	v_mov_b32_e32 v160, v159
	v_pk_add_f32 v[96:97], v[96:97], v[124:125]
	v_mov_b32_e32 v132, v131
	v_pk_add_f32 v[82:83], v[82:83], v[110:111]
	v_mov_b32_e32 v111, v64
	v_pk_add_f32 v[30:31], v[30:31], v[60:61]
	v_mov_b32_e32 v64, v63
	v_and_b32_e32 v37, 0xffff0000, v101
	v_and_b32_e32 v36, 0xffff0000, v100
	s_waitcnt vmcnt(8)
	v_and_b32_e32 v47, 0xffff0000, v107
	v_and_b32_e32 v46, 0xffff0000, v106
	v_pk_mul_f32 v[32:33], v[32:33], s[22:23] op_sel_hi:[1,0]
	v_pk_add_f32 v[68:69], v[68:69], v[160:161]
	v_pk_add_f32 v[96:97], v[96:97], v[132:133]
	v_mov_b32_e32 v140, v139
	v_pk_add_f32 v[30:31], v[30:31], v[64:65]
	v_pk_mul_f32 v[46:47], v[46:47], s[22:23] op_sel_hi:[1,0]
	v_pk_fma_f32 v[32:33], v[66:67], s[20:21], v[32:33] op_sel_hi:[1,0,1]
	v_pk_mul_f32 v[36:37], v[36:37], s[22:23] op_sel_hi:[1,0]
	v_pk_add_f32 v[96:97], v[96:97], v[140:141]
	v_mov_b32_e32 v148, v147
	v_pk_fma_f32 v[30:31], v[30:31], s[20:21], v[46:47] op_sel_hi:[1,0,1]
	v_pk_fma_f32 v[36:37], v[68:69], s[20:21], v[36:37] op_sel_hi:[1,0,1]
	v_add_f32_e32 v46, 0, v32
	v_pk_add_f32 v[96:97], v[96:97], v[148:149]
	v_mov_b32_e32 v156, v155
	v_lshlrev_b32_e32 v41, 16, v103
	v_lshlrev_b32_e32 v40, 16, v102
	v_add_f32_e32 v46, v36, v46
	v_pk_add_f32 v[96:97], v[96:97], v[156:157]
	v_mov_b32_e32 v164, v163
	v_and_b32_e32 v45, 0xffff0000, v103
	v_and_b32_e32 v44, 0xffff0000, v102
	v_add_f32_e32 v46, v33, v46
	v_pk_mul_f32 v[40:41], v[40:41], s[22:23] op_sel_hi:[1,0]
	v_pk_add_f32 v[96:97], v[96:97], v[164:165]
	v_add_f32_e32 v54, v37, v46
	v_pk_fma_f32 v[40:41], v[76:77], s[20:21], v[40:41] op_sel_hi:[1,0,1]
	v_pk_mul_f32 v[44:45], v[44:45], s[22:23] op_sel_hi:[1,0]
	s_waitcnt vmcnt(7)
; __device__ __forceinline__ void ph_combine(const Args& a, const bf16_t* X, const float* g, const float* b, bf16_t* Xo, float* outf) {
;     ...
;         float s = 0.f;
; #pragma unroll
;         for (int j = 0; j < 16; ++j) s += v[j];
;         const float mean = wave_sum(s) * (1.0f / 1024.0f);
;         float q = 0.f;
; #pragma unroll
;         for (int j = 0; j < 16; ++j) { v[j] -= mean; q += v[j] * v[j]; }
;         const float rstd = rsqrtf(wave_sum(q) * (1.0f / 1024.0f) + LN_EPS);
;         float o[16];
; #pragma unroll
;         for (int j = 0; j < 8; ++j) { o[j] = v[j] * rstd * g[lane * 8 + j] + b[lane * 8 + j]; o[8 + j] = v[8 + j] * rstd * g[512 + lane * 8 + j] + b[512 + lane * 8 + j]; }
;         if (outf) {
;             float* op = outf + (size_t)row * 1024;
;             *(float4*)(op + lane * 8) = make_float4(o[0], o[1], o[2], o[3]); *(float4*)(op + lane * 8 + 4) = make_float4(o[4], o[5], o[6], o[7]);
;             *(float4*)(op + 512 + lane * 8) = make_float4(o[8], o[9], o[10], o[11]); *(float4*)(op + 512 + lane * 8 + 4) = make_float4(o[12], o[13], o[14], o[15]);
	v_mov_b32_e32 v52, v0
	v_pk_fma_f32 v[44:45], v[96:97], s[20:21], v[44:45] op_sel_hi:[1,0,1]
	v_add_f32_e32 v0, v40, v54
	v_lshlrev_b32_e32 v35, 16, v105
	v_lshlrev_b32_e32 v34, 16, v104
	v_add_f32_e32 v0, v44, v0
	v_and_b32_e32 v39, 0xffff0000, v105
	v_and_b32_e32 v38, 0xffff0000, v104
	v_pk_mul_f32 v[34:35], v[34:35], s[22:23] op_sel_hi:[1,0]
	v_add_f32_e32 v0, v41, v0
	v_pk_fma_f32 v[34:35], v[108:109], s[20:21], v[34:35] op_sel_hi:[1,0,1]
	v_pk_mul_f32 v[38:39], v[38:39], s[22:23] op_sel_hi:[1,0]
	v_add_f32_e32 v0, v45, v0
	v_pk_fma_f32 v[38:39], v[74:75], s[20:21], v[38:39] op_sel_hi:[1,0,1]
	v_add_f32_e32 v0, v34, v0
	v_mov_b32_e32 v110, v62
	v_lshlrev_b32_e32 v43, 16, v107
	v_lshlrev_b32_e32 v42, 16, v106
	v_add_f32_e32 v0, v38, v0
	v_pk_add_f32 v[82:83], v[82:83], v[110:111]
	v_pk_mul_f32 v[42:43], v[42:43], s[22:23] op_sel_hi:[1,0]
	v_add_f32_e32 v0, v35, v0
	v_pk_fma_f32 v[42:43], v[82:83], s[20:21], v[42:43] op_sel_hi:[1,0,1]
	v_add_f32_e32 v0, v39, v0
	v_add_f32_e32 v0, v42, v0
	v_add_f32_e32 v0, v30, v0
	v_add_f32_e32 v0, v43, v0
	v_add_f32_e32 v0, v31, v0
	v_mov_b32_e32 v53, v2
	s_waitcnt vmcnt(6)
	v_mov_b32_e32 v48, v8
	v_add_f32_dpp v0, v0, v0 quad_perm:[1,0,3,2] row_mask:0xf bank_mask:0xf bound_ctrl:1
	v_mov_b32_e32 v49, v10
	v_mov_b32_e32 v10, v9
	v_add_f32_dpp v0, v0, v0 quad_perm:[2,3,0,1] row_mask:0xf bank_mask:0xf bound_ctrl:1
	s_waitcnt vmcnt(4)
	v_mov_b32_e32 v8, v84
	v_mov_b32_e32 v9, v86
	v_add_f32_dpp v0, v0, v0 row_half_mirror row_mask:0xf bank_mask:0xf bound_ctrl:1
	v_mov_b32_e32 v86, v85
	s_waitcnt vmcnt(2)
	v_mov_b32_e32 v46, v78
	v_add_f32_dpp v0, v0, v0 row_mirror row_mask:0xf bank_mask:0xf bound_ctrl:1
	v_mov_b32_e32 v47, v80
	v_readlane_b32 s29, v0, 16
	v_readlane_b32 s30, v0, 48
	v_readlane_b32 s24, v0, 0
	v_readlane_b32 s25, v0, 32
	v_mov_b32_e32 v54, s29
	v_mov_b32_e32 v55, s30
	v_pk_add_f32 v[54:55], s[24:25], v[54:55]
	v_mov_b32_e32 v80, v79
	v_add_f32_e32 v0, v54, v55
	v_mul_f32_e32 v0, 0x3a800000, v0
	v_pk_add_f32 v[32:33], v[32:33], v[0:1] op_sel_hi:[1,0] neg_lo:[0,1] neg_hi:[0,1]
	v_pk_add_f32 v[36:37], v[36:37], v[0:1] op_sel_hi:[1,0] neg_lo:[0,1] neg_hi:[0,1]
	v_pk_mul_f32 v[54:55], v[32:33], v[32:33]
	v_pk_mul_f32 v[56:57], v[36:37], v[36:37]
	v_pk_add_f32 v[40:41], v[40:41], v[0:1] op_sel_hi:[1,0] neg_lo:[0,1] neg_hi:[0,1]
	v_pk_add_f32 v[44:45], v[44:45], v[0:1] op_sel_hi:[1,0] neg_lo:[0,1] neg_hi:[0,1]
	v_pk_add_f32 v[34:35], v[34:35], v[0:1] op_sel_hi:[1,0] neg_lo:[0,1] neg_hi:[0,1]
	v_pk_add_f32 v[38:39], v[38:39], v[0:1] op_sel_hi:[1,0] neg_lo:[0,1] neg_hi:[0,1]
	v_pk_add_f32 v[42:43], v[42:43], v[0:1] op_sel_hi:[1,0] neg_lo:[0,1] neg_hi:[0,1]
	v_pk_add_f32 v[64:65], v[30:31], v[0:1] op_sel_hi:[1,0] neg_lo:[0,1] neg_hi:[0,1]
	v_add_f32_e32 v0, v54, v56
	v_add_f32_e32 v0, v55, v0
	v_pk_mul_f32 v[58:59], v[40:41], v[40:41]
	v_add_f32_e32 v0, v57, v0
	v_pk_mul_f32 v[60:61], v[44:45], v[44:45]
	v_add_f32_e32 v0, v58, v0
	v_add_f32_e32 v0, v60, v0
	v_add_f32_e32 v0, v59, v0
	v_add_f32_e32 v0, v61, v0
	v_mov_b32_e32 v62, v39
	v_mov_b32_e32 v63, v35
	v_fmac_f32_e32 v0, v34, v34
	v_pk_mul_f32 v[62:63], v[62:63], v[62:63]
	v_fmac_f32_e32 v0, v38, v38
	v_mov_b32_e32 v30, v64
	v_mov_b32_e32 v31, v42
	v_add_f32_e32 v0, v63, v0
	v_pk_mul_f32 v[30:31], v[30:31], v[30:31]
	v_add_f32_e32 v0, v62, v0
	v_mov_b32_e32 v66, v65
	v_mov_b32_e32 v67, v43
	v_add_f32_e32 v0, v31, v0
	v_pk_mul_f32 v[66:67], v[66:67], v[66:67]
	v_add_f32_e32 v0, v30, v0
	v_add_f32_e32 v0, v67, v0
	v_add_f32_e32 v0, v66, v0
	v_mov_b32_e32 v54, v4
	s_waitcnt vmcnt(0)
	v_mov_b32_e32 v50, v92
	v_add_f32_dpp v0, v0, v0 quad_perm:[1,0,3,2] row_mask:0xf bank_mask:0xf bound_ctrl:1
	v_mov_b32_e32 v51, v94
	v_mov_b32_e32 v94, v93
	v_add_f32_dpp v0, v0, v0 quad_perm:[2,3,0,1] row_mask:0xf bank_mask:0xf bound_ctrl:1
	v_mov_b32_e32 v55, v6
	v_mov_b32_e32 v6, v5
	v_add_f32_dpp v0, v0, v0 row_half_mirror row_mask:0xf bank_mask:0xf bound_ctrl:1
	s_nop 1
	v_add_f32_dpp v0, v0, v0 row_mirror row_mask:0xf bank_mask:0xf bound_ctrl:1
	s_nop 0
	v_readlane_b32 s29, v0, 16
	v_readlane_b32 s30, v0, 48
	v_readlane_b32 s24, v0, 0
	v_readlane_b32 s25, v0, 32
	v_mov_b32_e32 v30, s29
	v_mov_b32_e32 v31, s30
	v_pk_add_f32 v[30:31], s[24:25], v[30:31]
	s_nop 0
	v_add_f32_e32 v0, v30, v31
	v_fmamk_f32 v0, v0, 0x3a800000, v13
	v_mul_f32_e32 v2, 0x4b800000, v0
	v_cmp_gt_f32_e32 vcc, s26, v0
	s_nop 1
	v_cndmask_b32_e32 v0, v0, v2, vcc
	v_rsq_f32_e32 v0, v0
	v_mov_b32_e32 v2, v1
	v_mul_f32_e32 v1, 0x45800000, v0
	v_cndmask_b32_e32 v4, v0, v1, vcc
	v_pk_mul_f32 v[0:1], v[32:33], v[4:5] op_sel_hi:[1,0]
	v_pk_mul_f32 v[32:33], v[34:35], v[4:5] op_sel_hi:[1,0]
	v_pk_mul_f32 v[34:35], v[36:37], v[4:5] op_sel_hi:[1,0]
	v_pk_mul_f32 v[36:37], v[38:39], v[4:5] op_sel_hi:[1,0]
	v_pk_fma_f32 v[30:31], v[46:47], v[0:1], v[50:51]
	v_pk_fma_f32 v[0:1], v[48:49], v[32:33], v[8:9]
	v_pk_fma_f32 v[32:33], v[80:81], v[34:35], v[94:95]
	v_pk_fma_f32 v[8:9], v[10:11], v[36:37], v[86:87]
	v_pk_mul_f32 v[10:11], v[40:41], v[4:5] op_sel_hi:[1,0]
	v_mov_b32_e32 v34, v70
	v_mov_b32_e32 v35, v72
	v_pk_mul_f32 v[36:37], v[42:43], v[4:5] op_sel_hi:[1,0]
	v_pk_mul_f32 v[38:39], v[44:45], v[4:5] op_sel_hi:[1,0]
	v_mov_b32_e32 v72, v71
	v_pk_mul_f32 v[40:41], v[64:65], v[4:5] op_sel_hi:[1,0]
	v_mov_b32_e32 v42, v88
	v_mov_b32_e32 v43, v90
	v_mov_b32_e32 v90, v89
	v_pk_fma_f32 v[34:35], v[10:11], v[34:35], v[42:43]
	v_pk_fma_f32 v[10:11], v[36:37], v[52:53], v[54:55]
	v_pk_fma_f32 v[36:37], v[38:39], v[72:73], v[90:91]
	s_and_b64 vcc, exec, s[4:5]
	v_pk_fma_f32 v[2:3], v[40:41], v[2:3], v[6:7]
	s_cbranch_vccnz .LBB0_2920
	v_mov_b32_e32 v4, v30
	v_mov_b32_e32 v5, v32
	v_mov_b32_e32 v6, v31
	v_mov_b32_e32 v7, v33
	global_store_dwordx4 v[28:29], v[4:7], off nt
	s_nop 1
	v_mov_b32_e32 v4, v34
	v_mov_b32_e32 v5, v36
	v_mov_b32_e32 v6, v35
	v_mov_b32_e32 v7, v37
	global_store_dwordx4 v[28:29], v[4:7], off offset:16 nt
	s_nop 1
	v_mov_b32_e32 v4, v0
	v_mov_b32_e32 v5, v8
	v_mov_b32_e32 v6, v1
	v_mov_b32_e32 v7, v9
	global_store_dwordx4 v[28:29], v[4:7], off offset:2048 nt
	s_nop 1
	v_mov_b32_e32 v4, v10
	v_mov_b32_e32 v5, v2
	v_mov_b32_e32 v6, v11
	v_mov_b32_e32 v7, v3
	global_store_dwordx4 v[28:29], v[4:7], off offset:2064 nt
	s_cbranch_execnz .LBB0_2917
	s_branch .LBB0_2916
